# speedup vs baseline: 1.0174x; 1.0077x over previous
.Lg_s3skip0:
	s_cmp_eq_u32 s10, 10
	s_cselect_b32 s32, s46, s32
	s_sub_u32 s18, s10, 4
	s_cmp_lt_u32 s18, s9
	s_cselect_b32 s19, s32, 0x80000000
	ds_read_b128 v[226:229], v245 offset:0
	s_add_u32 s32, s32, 0x40000
	v_readlane_b32 s13, v247, s18
	v_lshrrev_b32_e32 v249, 4, v1
	v_lshlrev_b32_e32 v249, 3, v249
	v_lshrrev_b32_e64 v249, v249, s13
	v_and_b32_e32 v249, 0xff, v249
	v_cmp_eq_u32_e32 vcc, 1, v249
	s_nop 1
	v_cndmask_b32_e32 v249, v255, v246, vcc
	s_waitcnt lgkmcnt(0)
	buffer_store_dwordx4 v[226:229], v249, s[28:31], s19 offen sc0 sc1
	s_barrier
	s_add_u32 s10, s10, 1
	s_cmp_ge_u32 s10, s11
	s_cbranch_scc1 .Lg_end

.Lg_s3skip1:
	s_cmp_eq_u32 s10, 10
	s_cselect_b32 s32, s46, s32
	s_sub_u32 s18, s10, 4
	s_cmp_lt_u32 s18, s9
	s_cselect_b32 s19, s32, 0x80000000
	ds_read_b128 v[226:229], v245 offset:4352
	s_add_u32 s32, s32, 0x40000
	v_readlane_b32 s13, v247, s18
	v_lshrrev_b32_e32 v249, 4, v1
	v_lshlrev_b32_e32 v249, 3, v249
	v_lshrrev_b32_e64 v249, v249, s13
	v_and_b32_e32 v249, 0xff, v249
	v_cmp_eq_u32_e32 vcc, 1, v249
	s_nop 1
	v_cndmask_b32_e32 v249, v255, v246, vcc
	s_waitcnt lgkmcnt(0)
	buffer_store_dwordx4 v[226:229], v249, s[28:31], s19 offen sc0 sc1
	s_barrier
	s_add_u32 s10, s10, 1
	s_cmp_lt_u32 s10, s11
	s_cbranch_scc1 .Lg_top
